# speedup vs baseline: 1.0291x; 1.0033x over previous
.Lit_Af:
	v_add_u32_sdwa v88, v116, v42 dst_sel:DWORD dst_unused:UNUSED_PAD src0_sel:DWORD src1_sel:WORD_0
	v_add_u32_sdwa v89, v116, v42 dst_sel:DWORD dst_unused:UNUSED_PAD src0_sel:DWORD src1_sel:WORD_1
	ds_read_b64 v[68:69], v88
	v_add_u32_sdwa v90, v116, v43 dst_sel:DWORD dst_unused:UNUSED_PAD src0_sel:DWORD src1_sel:WORD_0
	ds_read_b64 v[70:71], v89
	v_add_u32_sdwa v91, v116, v43 dst_sel:DWORD dst_unused:UNUSED_PAD src0_sel:DWORD src1_sel:WORD_1
	ds_read_b64 v[72:73], v90
	ds_read_b64 v[74:75], v91
	v_add_u32_sdwa v92, v105, v52 dst_sel:DWORD dst_unused:UNUSED_PAD src0_sel:DWORD src1_sel:WORD_0
	v_add_u32_sdwa v93, v105, v52 dst_sel:DWORD dst_unused:UNUSED_PAD src0_sel:DWORD src1_sel:WORD_1
	v_add_u32_sdwa v106, v105, v53 dst_sel:DWORD dst_unused:UNUSED_PAD src0_sel:DWORD src1_sel:WORD_0
	v_add_u32_sdwa v107, v105, v53 dst_sel:DWORD dst_unused:UNUSED_PAD src0_sel:DWORD src1_sel:WORD_1
	v_add_u32_sdwa v108, v105, v54 dst_sel:DWORD dst_unused:UNUSED_PAD src0_sel:DWORD src1_sel:WORD_0
	v_add_u32_sdwa v109, v105, v54 dst_sel:DWORD dst_unused:UNUSED_PAD src0_sel:DWORD src1_sel:WORD_1
	v_add_u32_sdwa v88, v105, v55 dst_sel:DWORD dst_unused:UNUSED_PAD src0_sel:DWORD src1_sel:WORD_0
	v_add_u32_sdwa v89, v105, v55 dst_sel:DWORD dst_unused:UNUSED_PAD src0_sel:DWORD src1_sel:WORD_1
	ds_read_b128 v[120:123], v92
	ds_read_b128 v[124:127], v93
	ds_read_b128 v[128:131], v106
	ds_read_b128 v[132:135], v107
	ds_read_b128 v[140:143], v108
	ds_read_b128 v[144:147], v109
	ds_read_b128 v[148:151], v88
	ds_read_b128 v[152:155], v89
	v_add_u32_sdwa v118, v116, v39 dst_sel:DWORD dst_unused:UNUSED_PAD src0_sel:DWORD src1_sel:WORD_0
	s_waitcnt lgkmcnt(11)
	v_pk_add_f32 v[76:77], v[44:45], v[68:69]
	s_waitcnt lgkmcnt(9)
	v_pk_add_f32 v[78:79], v[70:71], v[72:73]
	s_waitcnt lgkmcnt(8)
	v_pk_add_f32 v[76:77], v[76:77], v[74:75]
	v_bfe_u32 v117, v41, 16, 7
	v_pk_add_f32 v[76:77], v[76:77], v[78:79]
	v_add_u32_sdwa v119, v116, v39 dst_sel:DWORD dst_unused:UNUSED_PAD src0_sel:DWORD src1_sel:WORD_1
	v_pk_mul_f32 v[78:79], v[40:41], v[76:77] op_sel_hi:[0,1]
	v_add_u32_sdwa v136, v116, v41 dst_sel:DWORD dst_unused:UNUSED_PAD src0_sel:DWORD src1_sel:WORD_0
	ds_write_b64 v137, v[78:79]
	ds_read_b128 v[46:49], v138 offset:56896
	ds_read_b64 v[50:51], v139
	ds_read2_b64 v[56:59], v156 offset1:2
	ds_read_b32 v60, v157
	v_cmp_eq_u32_e64 s[6:7], 1, v117
	s_waitcnt lgkmcnt(4)
	s_mov_b64 exec, s[6:7]
	ds_read_b64 v[82:83], v118
	ds_read_b64 v[84:85], v119
	ds_read_b64 v[86:87], v136
	s_mov_b64 exec, -1
	v_pk_add_f32 v[120:121], v[120:121], v[124:125]
	v_pk_add_f32 v[122:123], v[122:123], v[126:127]
	v_pk_add_f32 v[128:129], v[128:129], v[132:133]
	v_pk_add_f32 v[130:131], v[130:131], v[134:135]
	v_pk_add_f32 v[140:141], v[140:141], v[144:145]
	v_pk_add_f32 v[142:143], v[142:143], v[146:147]
	v_pk_add_f32 v[148:149], v[148:149], v[152:153]
	v_pk_add_f32 v[150:151], v[150:151], v[154:155]
	v_pk_add_f32 v[120:121], v[120:121], v[128:129]
	v_pk_add_f32 v[122:123], v[122:123], v[130:131]
	v_pk_add_f32 v[140:141], v[140:141], v[148:149]
	v_pk_add_f32 v[142:143], v[142:143], v[150:151]
	v_pk_add_f32 v[120:121], v[120:121], v[140:141]
	v_pk_add_f32 v[122:123], v[122:123], v[142:143]
	v_add_u32_e32 v138, 0xfffffe00, v138
	v_add_u32_e32 v139, 0xffffff00, v139
	v_permlane32_swap_b32_e32 v120, v122
	v_permlane32_swap_b32_e32 v121, v123
	v_pk_add_f32 v[62:63], v[120:121], v[122:123]
	s_mov_b64 exec, s[6:7]
	s_waitcnt lgkmcnt(2)
	v_pk_fma_f32 v[80:81], v[40:41], v[82:83], v[78:79] op_sel_hi:[0,1,1]
	s_waitcnt lgkmcnt(1)
	v_pk_fma_f32 v[80:81], v[40:41], v[84:85], v[80:81] op_sel_hi:[0,1,1]
	s_waitcnt lgkmcnt(0)
	v_pk_fma_f32 v[80:81], v[40:41], v[86:87], v[80:81] op_sel_hi:[0,1,1]
	ds_write_b64 v137, v[80:81]
	s_mov_b64 exec, -1
	s_cmp_lt_u32 s9, 2
	s_cbranch_scc1 .Lend_A
	s_mov_b32 s8, 2

.Lend_A:
	s_waitcnt lgkmcnt(0)
	v_add_u32_e32 v156, 0xfffffa00, v156
	v_add_u32_e32 v157, -4, v157
	v_add_u32_e32 v137, 0xfffffe00, v137
	v_max_i32_e32 v156, v156, v162
	v_lshl_add_u64 v[158:159], v[158:159], 0, s[2:3]
	v_readfirstlane_b32 s4, v60
	s_sub_u32 s5, s5, 1
	s_or_b32 s10, s21, s4
	s_and_b32 s10, s10, 0x700
	s_cbranch_scc1 .Lit_Bs
	s_and_b32 s9, s21, 0xff
	s_cbranch_scc0 .Lit_Bs
.Lit_Bf:
	v_add_u32_sdwa v88, v116, v50 dst_sel:DWORD dst_unused:UNUSED_PAD src0_sel:DWORD src1_sel:WORD_0
	v_add_u32_sdwa v89, v116, v50 dst_sel:DWORD dst_unused:UNUSED_PAD src0_sel:DWORD src1_sel:WORD_1
	ds_read_b64 v[68:69], v88
	v_add_u32_sdwa v90, v116, v51 dst_sel:DWORD dst_unused:UNUSED_PAD src0_sel:DWORD src1_sel:WORD_0
	ds_read_b64 v[70:71], v89
	v_add_u32_sdwa v91, v116, v51 dst_sel:DWORD dst_unused:UNUSED_PAD src0_sel:DWORD src1_sel:WORD_1
	ds_read_b64 v[72:73], v90
	ds_read_b64 v[74:75], v91
	v_add_u32_sdwa v92, v105, v56 dst_sel:DWORD dst_unused:UNUSED_PAD src0_sel:DWORD src1_sel:WORD_0
	v_add_u32_sdwa v93, v105, v56 dst_sel:DWORD dst_unused:UNUSED_PAD src0_sel:DWORD src1_sel:WORD_1
	v_add_u32_sdwa v106, v105, v57 dst_sel:DWORD dst_unused:UNUSED_PAD src0_sel:DWORD src1_sel:WORD_0
	v_add_u32_sdwa v107, v105, v57 dst_sel:DWORD dst_unused:UNUSED_PAD src0_sel:DWORD src1_sel:WORD_1
	v_add_u32_sdwa v108, v105, v58 dst_sel:DWORD dst_unused:UNUSED_PAD src0_sel:DWORD src1_sel:WORD_0
	v_add_u32_sdwa v109, v105, v58 dst_sel:DWORD dst_unused:UNUSED_PAD src0_sel:DWORD src1_sel:WORD_1
	v_add_u32_sdwa v88, v105, v59 dst_sel:DWORD dst_unused:UNUSED_PAD src0_sel:DWORD src1_sel:WORD_0
	v_add_u32_sdwa v89, v105, v59 dst_sel:DWORD dst_unused:UNUSED_PAD src0_sel:DWORD src1_sel:WORD_1
	ds_read_b128 v[120:123], v92
	ds_read_b128 v[124:127], v93
	ds_read_b128 v[128:131], v106
	ds_read_b128 v[132:135], v107
	ds_read_b128 v[140:143], v108
	ds_read_b128 v[144:147], v109
	ds_read_b128 v[148:151], v88
	ds_read_b128 v[152:155], v89
	v_add_u32_sdwa v118, v116, v47 dst_sel:DWORD dst_unused:UNUSED_PAD src0_sel:DWORD src1_sel:WORD_0
	s_waitcnt lgkmcnt(11)
	v_pk_add_f32 v[76:77], v[62:63], v[68:69]
	s_waitcnt lgkmcnt(9)
	v_pk_add_f32 v[78:79], v[70:71], v[72:73]
	s_waitcnt lgkmcnt(8)
	v_pk_add_f32 v[76:77], v[76:77], v[74:75]
	v_bfe_u32 v117, v49, 16, 7
	v_pk_add_f32 v[76:77], v[76:77], v[78:79]
	v_add_u32_sdwa v119, v116, v47 dst_sel:DWORD dst_unused:UNUSED_PAD src0_sel:DWORD src1_sel:WORD_1
	v_pk_mul_f32 v[78:79], v[48:49], v[76:77] op_sel_hi:[0,1]
	v_add_u32_sdwa v136, v116, v49 dst_sel:DWORD dst_unused:UNUSED_PAD src0_sel:DWORD src1_sel:WORD_0
	ds_write_b64 v137, v[78:79]
	ds_read_b128 v[38:41], v138 offset:56896
	ds_read_b64 v[42:43], v139
	ds_read2_b64 v[52:55], v156 offset1:2
	ds_read_b32 v60, v157
	v_cmp_eq_u32_e64 s[6:7], 1, v117
	s_waitcnt lgkmcnt(4)
	s_mov_b64 exec, s[6:7]
	ds_read_b64 v[82:83], v118
	ds_read_b64 v[84:85], v119
	ds_read_b64 v[86:87], v136
	s_mov_b64 exec, -1
	v_pk_add_f32 v[120:121], v[120:121], v[124:125]
	v_pk_add_f32 v[122:123], v[122:123], v[126:127]
	v_pk_add_f32 v[128:129], v[128:129], v[132:133]
	v_pk_add_f32 v[130:131], v[130:131], v[134:135]
	v_pk_add_f32 v[140:141], v[140:141], v[144:145]
	v_pk_add_f32 v[142:143], v[142:143], v[146:147]
	v_pk_add_f32 v[148:149], v[148:149], v[152:153]
	v_pk_add_f32 v[150:151], v[150:151], v[154:155]
	v_pk_add_f32 v[120:121], v[120:121], v[128:129]
	v_pk_add_f32 v[122:123], v[122:123], v[130:131]
	v_pk_add_f32 v[140:141], v[140:141], v[148:149]
	v_pk_add_f32 v[142:143], v[142:143], v[150:151]
	v_pk_add_f32 v[120:121], v[120:121], v[140:141]
	v_pk_add_f32 v[122:123], v[122:123], v[142:143]
	v_add_u32_e32 v138, 0xfffffe00, v138
	v_add_u32_e32 v139, 0xffffff00, v139
	v_permlane32_swap_b32_e32 v120, v122
	v_permlane32_swap_b32_e32 v121, v123
	v_pk_add_f32 v[44:45], v[120:121], v[122:123]
	s_mov_b64 exec, s[6:7]
	s_waitcnt lgkmcnt(2)
	v_pk_fma_f32 v[80:81], v[48:49], v[82:83], v[78:79] op_sel_hi:[0,1,1]
	s_waitcnt lgkmcnt(1)
	v_pk_fma_f32 v[80:81], v[48:49], v[84:85], v[80:81] op_sel_hi:[0,1,1]
	s_waitcnt lgkmcnt(0)
	v_pk_fma_f32 v[80:81], v[48:49], v[86:87], v[80:81] op_sel_hi:[0,1,1]
	ds_write_b64 v137, v[80:81]
	s_mov_b64 exec, -1
	s_cmp_lt_u32 s9, 2
	s_cbranch_scc1 .Lend_B
	s_mov_b32 s8, 2

.Lend_B:
	s_waitcnt lgkmcnt(0)
	v_add_u32_e32 v156, 0xfffffa00, v156
	v_add_u32_e32 v157, -4, v157
	v_add_u32_e32 v137, 0xfffffe00, v137
	v_max_i32_e32 v156, v156, v162
	v_lshl_add_u64 v[158:159], v[158:159], 0, s[2:3]
	v_readfirstlane_b32 s21, v60
	s_cmp_eq_u32 s5, 0
	s_cbranch_scc1 .Lchain_done
	s_sub_u32 s5, s5, 1
	s_branch .Lchain_top

.Lnearslow_ret_As:
	v_pk_mul_f32 v[78:79], v[40:41], v[76:77] op_sel_hi:[0,1]
	v_add_u32_sdwa v136, v116, v41 dst_sel:DWORD dst_unused:UNUSED_PAD src0_sel:DWORD src1_sel:WORD_0
	ds_write_b64 v137, v[78:79]
	ds_read_b128 v[46:49], v138 offset:56896
	ds_read_b64 v[50:51], v139
	ds_read2_b64 v[56:59], v156 offset1:2
	ds_read_b32 v60, v157
	s_and_b32 s9, s4, 0xff
	v_cmp_eq_u32_e64 s[6:7], 1, v117
	s_waitcnt lgkmcnt(4)
	s_bitcmp1_b32 s4, 9
	s_cbranch_scc1 .Lfs_As
	s_cmp_eq_u32 s9, 0
	s_cbranch_scc1 .Lfs_As
	s_mov_b64 exec, s[6:7]
	ds_read_b64 v[82:83], v118
	ds_read_b64 v[84:85], v119
	ds_read_b64 v[86:87], v136
	s_mov_b64 exec, -1

.Lfarslow_ret_As:
	v_pk_add_f32 v[120:121], v[120:121], v[128:129]
	v_pk_add_f32 v[122:123], v[122:123], v[130:131]
	v_pk_add_f32 v[140:141], v[140:141], v[148:149]
	v_pk_add_f32 v[142:143], v[142:143], v[150:151]
	v_pk_add_f32 v[120:121], v[120:121], v[140:141]
	v_pk_add_f32 v[122:123], v[122:123], v[142:143]
	v_add_u32_e32 v138, 0xfffffe00, v138
	v_add_u32_e32 v139, 0xffffff00, v139
	v_permlane32_swap_b32_e32 v120, v122
	v_permlane32_swap_b32_e32 v121, v123
	v_pk_add_f32 v[62:63], v[120:121], v[122:123]
	s_bitcmp1_b32 s4, 9
	s_cbranch_scc1 .Lslowlev_As
	s_cmp_eq_u32 s9, 0
	s_cbranch_scc1 .Lend_A
	s_mov_b64 exec, s[6:7]
	s_waitcnt lgkmcnt(2)
	v_pk_fma_f32 v[80:81], v[40:41], v[82:83], v[78:79] op_sel_hi:[0,1,1]
	s_waitcnt lgkmcnt(1)
	v_pk_fma_f32 v[80:81], v[40:41], v[84:85], v[80:81] op_sel_hi:[0,1,1]
	s_waitcnt lgkmcnt(0)
	v_pk_fma_f32 v[80:81], v[40:41], v[86:87], v[80:81] op_sel_hi:[0,1,1]
	ds_write_b64 v137, v[80:81]
	s_mov_b64 exec, -1
	s_cmp_lt_u32 s9, 2
	s_cbranch_scc1 .Lend_A
	s_mov_b32 s8, 2

.Lnearslow_ret_Bs:
	v_pk_mul_f32 v[78:79], v[48:49], v[76:77] op_sel_hi:[0,1]
	v_add_u32_sdwa v136, v116, v49 dst_sel:DWORD dst_unused:UNUSED_PAD src0_sel:DWORD src1_sel:WORD_0
	ds_write_b64 v137, v[78:79]
	ds_read_b128 v[38:41], v138 offset:56896
	ds_read_b64 v[42:43], v139
	ds_read2_b64 v[52:55], v156 offset1:2
	ds_read_b32 v60, v157
	s_and_b32 s9, s21, 0xff
	v_cmp_eq_u32_e64 s[6:7], 1, v117
	s_waitcnt lgkmcnt(4)
	s_bitcmp1_b32 s21, 9
	s_cbranch_scc1 .Lfs_Bs
	s_cmp_eq_u32 s9, 0
	s_cbranch_scc1 .Lfs_Bs
	s_mov_b64 exec, s[6:7]
	ds_read_b64 v[82:83], v118
	ds_read_b64 v[84:85], v119
	ds_read_b64 v[86:87], v136
	s_mov_b64 exec, -1

.Lfarslow_ret_Bs:
	v_pk_add_f32 v[120:121], v[120:121], v[128:129]
	v_pk_add_f32 v[122:123], v[122:123], v[130:131]
	v_pk_add_f32 v[140:141], v[140:141], v[148:149]
	v_pk_add_f32 v[142:143], v[142:143], v[150:151]
	v_pk_add_f32 v[120:121], v[120:121], v[140:141]
	v_pk_add_f32 v[122:123], v[122:123], v[142:143]
	v_add_u32_e32 v138, 0xfffffe00, v138
	v_add_u32_e32 v139, 0xffffff00, v139
	v_permlane32_swap_b32_e32 v120, v122
	v_permlane32_swap_b32_e32 v121, v123
	v_pk_add_f32 v[44:45], v[120:121], v[122:123]
	s_bitcmp1_b32 s21, 9
	s_cbranch_scc1 .Lslowlev_Bs
	s_cmp_eq_u32 s9, 0
	s_cbranch_scc1 .Lend_B
	s_mov_b64 exec, s[6:7]
	s_waitcnt lgkmcnt(2)
	v_pk_fma_f32 v[80:81], v[48:49], v[82:83], v[78:79] op_sel_hi:[0,1,1]
	s_waitcnt lgkmcnt(1)
	v_pk_fma_f32 v[80:81], v[48:49], v[84:85], v[80:81] op_sel_hi:[0,1,1]
	s_waitcnt lgkmcnt(0)
	v_pk_fma_f32 v[80:81], v[48:49], v[86:87], v[80:81] op_sel_hi:[0,1,1]
	ds_write_b64 v137, v[80:81]
	s_mov_b64 exec, -1
	s_cmp_lt_u32 s9, 2
	s_cbranch_scc1 .Lend_B
	s_mov_b32 s8, 2
